# v8 + expert-weight fp8 conversion of layers 2,3 deferred from prologue into idle att-half WGs of ut_att phase (P=64,Q=96)
# baseline (speedup 1.0000x reference)
.LBB0_654:
	s_barrier
	v_readlane_b32 s46, v255, 4
	s_sub_i32 s42, s88, 0x80
	s_lshl_b32 s42, s42, 3
	s_lshr_b32 s5, s33, 6
	s_add_i32 s42, s42, s5
	s_mul_i32 s5, s5, 0x4200
	s_movk_i32 s45, 96
	s_movk_i32 s4, 32
	s_movk_i32 vcc_lo, 64
	s_movk_i32 vcc_hi, 32
	s_cmp_eq_u32 s46, 1
	s_cselect_b32 s45, vcc_lo, s45
	s_cselect_b32 s4, vcc_hi, s4
	s_lshl_b32 s44, s4, 9
	s_mul_i32 s43, s4, 0x300
	v_readlane_b32 s8, v252, 0
	v_readlane_b32 s9, v252, 1
	v_mbcnt_lo_u32_b32 v13, -1, 0
	v_mbcnt_hi_u32_b32 v13, -1, v13
	s_load_dwordx2 s[6:7], s[8:9], 0xa0
	s_load_dwordx2 s[10:11], s[8:9], 0xd8
	s_load_dwordx2 s[8:9], s[8:9], 0xb0
	s_movk_i32 s46, 0x84
	s_movk_i32 s47, 0x840
	v_and_b32_e32 v14, 31, v13
	v_lshlrev_b32_e32 v14, 2, v14
	v_lshrrev_b32_e32 v15, 5, v13
	v_mov_b32_e32 v4, s5
	v_mad_u32_u24 v4, v15, s46, v4
	v_add_u32_e32 v4, v4, v14
	v_and_b32_e32 v10, 7, v13
	v_lshrrev_b32_e32 v11, 3, v13
	v_mov_b32_e32 v5, s5
	v_mad_u32_u24 v5, v10, s47, v5
	v_lshl_add_u32 v5, v11, 2, v5
	v_lshlrev_b32_e32 v6, 10, v11
	v_lshl_add_u32 v6, v10, 4, v6
	v_add_u32_e32 v7, 0x2000, v6
	v_add_u32_e32 v8, 0x4000, v6
	v_add_u32_e32 v9, 0x6000, v6
	s_waitcnt lgkmcnt(0)
	s_cmp_lt_u32 s42, s43
	s_cbranch_scc0 .Lcv_done
	s_cmp_lt_u32 s42, s44
	s_cbranch_scc0 .Lcv_dn0
	s_lshr_b32 s4, s42, 9
	s_add_i32 s4, s4, s45
	s_bfe_u32 s5, s42, 0x30006
	s_and_b32 vcc_lo, s42, 63
	s_lshl_b32 s46, s4, 23
	s_lshl_b32 s47, s5, 20
	s_add_u32 s46, s46, s47
	s_lshl_b32 s47, vcc_lo, 7
	s_add_u32 s46, s46, s47
	s_add_u32 s46, s46, s6
	s_addc_u32 s47, s7, 0
	s_lshl_b32 s52, s4, 21
	s_add_u32 s52, s52, 0x4400000
	s_lshl_b32 s53, s5, 7
	s_add_u32 s52, s52, s53
	s_bfe_u32 s53, vcc_lo, 0x30002
	s_lshl_b32 s53, s53, 18
	s_add_u32 s52, s52, s53
	s_lshr_b32 s53, vcc_lo, 5
	s_lshl_b32 s53, s53, 17
	s_add_u32 s52, s52, s53
	s_and_b32 s53, vcc_lo, 3
	s_lshl_b32 s53, s53, 15
	s_add_u32 s52, s52, s53
	s_add_u32 s52, s52, s10
	s_addc_u32 s53, s11, 0
	s_mov_b32 s51, 0x42000000
	s_movk_i32 s5, 0x2000
	s_movk_i32 s4, 0x4000
	s_branch .Lcv_ld0
.Lcv_dn0:
	s_sub_u32 vcc_hi, s42, s44
	s_lshr_b32 s4, vcc_hi, 8
	s_add_i32 s4, s4, s45
	s_bfe_u32 s5, vcc_hi, 0x30005
	s_and_b32 vcc_lo, vcc_hi, 31
	s_lshl_b32 s46, s4, 22
	s_lshl_b32 s47, s5, 19
	s_add_u32 s46, s46, s47
	s_lshl_b32 s47, vcc_lo, 7
	s_add_u32 s46, s46, s47
	s_add_u32 s46, s46, s8
	s_addc_u32 s47, s9, 0
	s_lshl_b32 s52, s4, 20
	s_add_u32 s52, s52, 0x24400000
	s_lshl_b32 s53, s5, 7
	s_add_u32 s52, s52, s53
	s_lshl_b32 s53, vcc_lo, 15
	s_add_u32 s52, s52, s53
	s_add_u32 s52, s52, s10
	s_addc_u32 s53, s11, 0
	s_mov_b32 s51, 0x42800000
	s_movk_i32 s5, 0x1000
	s_movk_i32 s4, 0x2000
.Lcv_ld0:
	v_mad_u32_u24 v12, v15, s5, v14
	global_load_dword v64, v12, s[46:47]
	s_add_u32 s46, s46, s4
	s_addc_u32 s47, s47, 0
	global_load_dword v65, v12, s[46:47]
	s_add_u32 s46, s46, s4
	s_addc_u32 s47, s47, 0
	global_load_dword v66, v12, s[46:47]
	s_add_u32 s46, s46, s4
	s_addc_u32 s47, s47, 0
	global_load_dword v67, v12, s[46:47]
	s_add_u32 s46, s46, s4
	s_addc_u32 s47, s47, 0
	global_load_dword v68, v12, s[46:47]
	s_add_u32 s46, s46, s4
	s_addc_u32 s47, s47, 0
	global_load_dword v69, v12, s[46:47]
	s_add_u32 s46, s46, s4
	s_addc_u32 s47, s47, 0
	global_load_dword v70, v12, s[46:47]
	s_add_u32 s46, s46, s4
	s_addc_u32 s47, s47, 0
	global_load_dword v71, v12, s[46:47]
	s_add_u32 s46, s46, s4
	s_addc_u32 s47, s47, 0
	global_load_dword v72, v12, s[46:47]
	s_add_u32 s46, s46, s4
	s_addc_u32 s47, s47, 0
	global_load_dword v73, v12, s[46:47]
	s_add_u32 s46, s46, s4
	s_addc_u32 s47, s47, 0
	global_load_dword v74, v12, s[46:47]
	s_add_u32 s46, s46, s4
	s_addc_u32 s47, s47, 0
	global_load_dword v75, v12, s[46:47]
	s_add_u32 s46, s46, s4
	s_addc_u32 s47, s47, 0
	global_load_dword v76, v12, s[46:47]
	s_add_u32 s46, s46, s4
	s_addc_u32 s47, s47, 0
	global_load_dword v77, v12, s[46:47]
	s_add_u32 s46, s46, s4
	s_addc_u32 s47, s47, 0
	global_load_dword v78, v12, s[46:47]
	s_add_u32 s46, s46, s4
	s_addc_u32 s47, s47, 0
	global_load_dword v79, v12, s[46:47]
	s_add_u32 s46, s46, s4
	s_addc_u32 s47, s47, 0
	global_load_dword v80, v12, s[46:47]
	s_add_u32 s46, s46, s4
	s_addc_u32 s47, s47, 0
	global_load_dword v81, v12, s[46:47]
	s_add_u32 s46, s46, s4
	s_addc_u32 s47, s47, 0
	global_load_dword v82, v12, s[46:47]
	s_add_u32 s46, s46, s4
	s_addc_u32 s47, s47, 0
	global_load_dword v83, v12, s[46:47]
	s_add_u32 s46, s46, s4
	s_addc_u32 s47, s47, 0
	global_load_dword v84, v12, s[46:47]
	s_add_u32 s46, s46, s4
	s_addc_u32 s47, s47, 0
	global_load_dword v85, v12, s[46:47]
	s_add_u32 s46, s46, s4
	s_addc_u32 s47, s47, 0
	global_load_dword v86, v12, s[46:47]
	s_add_u32 s46, s46, s4
	s_addc_u32 s47, s47, 0
	global_load_dword v87, v12, s[46:47]
	s_add_u32 s46, s46, s4
	s_addc_u32 s47, s47, 0
	global_load_dword v88, v12, s[46:47]
	s_add_u32 s46, s46, s4
	s_addc_u32 s47, s47, 0
	global_load_dword v89, v12, s[46:47]
	s_add_u32 s46, s46, s4
	s_addc_u32 s47, s47, 0
	global_load_dword v90, v12, s[46:47]
	s_add_u32 s46, s46, s4
	s_addc_u32 s47, s47, 0
	global_load_dword v91, v12, s[46:47]
	s_add_u32 s46, s46, s4
	s_addc_u32 s47, s47, 0
	global_load_dword v92, v12, s[46:47]
	s_add_u32 s46, s46, s4
	s_addc_u32 s47, s47, 0
	global_load_dword v93, v12, s[46:47]
	s_add_u32 s46, s46, s4
	s_addc_u32 s47, s47, 0
	global_load_dword v94, v12, s[46:47]
	s_add_u32 s46, s46, s4
	s_addc_u32 s47, s47, 0
	global_load_dword v95, v12, s[46:47]
	s_add_u32 s46, s46, s4
	s_addc_u32 s47, s47, 0
	global_load_dword v96, v12, s[46:47]
	s_add_u32 s46, s46, s4
	s_addc_u32 s47, s47, 0
	global_load_dword v97, v12, s[46:47]
	s_add_u32 s46, s46, s4
	s_addc_u32 s47, s47, 0
	global_load_dword v98, v12, s[46:47]
	s_add_u32 s46, s46, s4
	s_addc_u32 s47, s47, 0
	global_load_dword v99, v12, s[46:47]
	s_add_u32 s46, s46, s4
	s_addc_u32 s47, s47, 0
	global_load_dword v100, v12, s[46:47]
	s_add_u32 s46, s46, s4
	s_addc_u32 s47, s47, 0
	global_load_dword v101, v12, s[46:47]
	s_add_u32 s46, s46, s4
	s_addc_u32 s47, s47, 0
	global_load_dword v102, v12, s[46:47]
	s_add_u32 s46, s46, s4
	s_addc_u32 s47, s47, 0
	global_load_dword v103, v12, s[46:47]
	s_add_u32 s46, s46, s4
	s_addc_u32 s47, s47, 0
	global_load_dword v104, v12, s[46:47]
	s_add_u32 s46, s46, s4
	s_addc_u32 s47, s47, 0
	global_load_dword v105, v12, s[46:47]
	s_add_u32 s46, s46, s4
	s_addc_u32 s47, s47, 0
	global_load_dword v106, v12, s[46:47]
	s_add_u32 s46, s46, s4
	s_addc_u32 s47, s47, 0
	global_load_dword v107, v12, s[46:47]
	s_add_u32 s46, s46, s4
	s_addc_u32 s47, s47, 0
	global_load_dword v108, v12, s[46:47]
	s_add_u32 s46, s46, s4
	s_addc_u32 s47, s47, 0
	global_load_dword v109, v12, s[46:47]
	s_add_u32 s46, s46, s4
	s_addc_u32 s47, s47, 0
	global_load_dword v110, v12, s[46:47]
	s_add_u32 s46, s46, s4
	s_addc_u32 s47, s47, 0
	global_load_dword v111, v12, s[46:47]
	s_add_u32 s46, s46, s4
	s_addc_u32 s47, s47, 0
	global_load_dword v112, v12, s[46:47]
	s_add_u32 s46, s46, s4
	s_addc_u32 s47, s47, 0
	global_load_dword v113, v12, s[46:47]
	s_add_u32 s46, s46, s4
	s_addc_u32 s47, s47, 0
	global_load_dword v114, v12, s[46:47]
	s_add_u32 s46, s46, s4
	s_addc_u32 s47, s47, 0
	global_load_dword v115, v12, s[46:47]
	s_add_u32 s46, s46, s4
	s_addc_u32 s47, s47, 0
	global_load_dword v116, v12, s[46:47]
	s_add_u32 s46, s46, s4
	s_addc_u32 s47, s47, 0
	global_load_dword v117, v12, s[46:47]
	s_add_u32 s46, s46, s4
	s_addc_u32 s47, s47, 0
	global_load_dword v118, v12, s[46:47]
	s_add_u32 s46, s46, s4
	s_addc_u32 s47, s47, 0
	global_load_dword v119, v12, s[46:47]
	s_add_u32 s46, s46, s4
	s_addc_u32 s47, s47, 0
	global_load_dword v120, v12, s[46:47]
	s_add_u32 s46, s46, s4
	s_addc_u32 s47, s47, 0
	global_load_dword v121, v12, s[46:47]
	s_add_u32 s46, s46, s4
	s_addc_u32 s47, s47, 0
	global_load_dword v122, v12, s[46:47]
	s_add_u32 s46, s46, s4
	s_addc_u32 s47, s47, 0
	global_load_dword v123, v12, s[46:47]
	s_add_u32 s46, s46, s4
	s_addc_u32 s47, s47, 0
	global_load_dword v124, v12, s[46:47]
	s_add_u32 s46, s46, s4
	s_addc_u32 s47, s47, 0
	global_load_dword v125, v12, s[46:47]
	s_add_u32 s46, s46, s4
	s_addc_u32 s47, s47, 0
	global_load_dword v126, v12, s[46:47]
	s_add_u32 s46, s46, s4
	s_addc_u32 s47, s47, 0
	global_load_dword v127, v12, s[46:47]
	s_waitcnt vmcnt(0)
	s_branch .Lcv_body
.Lcv_loop:
	s_waitcnt vmcnt(4)
.Lcv_body:
	s_mov_b64 s[48:49], s[52:53]
	s_mov_b32 s50, s51
	ds_write_b32 v4, v64
	ds_write_b32 v4, v65 offset:264
	ds_write_b32 v4, v66 offset:528
	ds_write_b32 v4, v67 offset:792
	ds_write_b32 v4, v68 offset:1056
	ds_write_b32 v4, v69 offset:1320
	ds_write_b32 v4, v70 offset:1584
	ds_write_b32 v4, v71 offset:1848
	ds_write_b32 v4, v72 offset:2112
	ds_write_b32 v4, v73 offset:2376
	ds_write_b32 v4, v74 offset:2640
	ds_write_b32 v4, v75 offset:2904
	ds_write_b32 v4, v76 offset:3168
	ds_write_b32 v4, v77 offset:3432
	ds_write_b32 v4, v78 offset:3696
	ds_write_b32 v4, v79 offset:3960
	ds_write_b32 v4, v80 offset:4224
	ds_write_b32 v4, v81 offset:4488
	ds_write_b32 v4, v82 offset:4752
	ds_write_b32 v4, v83 offset:5016
	ds_write_b32 v4, v84 offset:5280
	ds_write_b32 v4, v85 offset:5544
	ds_write_b32 v4, v86 offset:5808
	ds_write_b32 v4, v87 offset:6072
	ds_write_b32 v4, v88 offset:6336
	ds_write_b32 v4, v89 offset:6600
	ds_write_b32 v4, v90 offset:6864
	ds_write_b32 v4, v91 offset:7128
	ds_write_b32 v4, v92 offset:7392
	ds_write_b32 v4, v93 offset:7656
	ds_write_b32 v4, v94 offset:7920
	ds_write_b32 v4, v95 offset:8184
	ds_write_b32 v4, v96 offset:8448
	ds_write_b32 v4, v97 offset:8712
	ds_write_b32 v4, v98 offset:8976
	ds_write_b32 v4, v99 offset:9240
	ds_write_b32 v4, v100 offset:9504
	ds_write_b32 v4, v101 offset:9768
	ds_write_b32 v4, v102 offset:10032
	ds_write_b32 v4, v103 offset:10296
	ds_write_b32 v4, v104 offset:10560
	ds_write_b32 v4, v105 offset:10824
	ds_write_b32 v4, v106 offset:11088
	ds_write_b32 v4, v107 offset:11352
	ds_write_b32 v4, v108 offset:11616
	ds_write_b32 v4, v109 offset:11880
	ds_write_b32 v4, v110 offset:12144
	ds_write_b32 v4, v111 offset:12408
	ds_write_b32 v4, v112 offset:12672
	ds_write_b32 v4, v113 offset:12936
	ds_write_b32 v4, v114 offset:13200
	ds_write_b32 v4, v115 offset:13464
	ds_write_b32 v4, v116 offset:13728
	ds_write_b32 v4, v117 offset:13992
	ds_write_b32 v4, v118 offset:14256
	ds_write_b32 v4, v119 offset:14520
	ds_write_b32 v4, v120 offset:14784
	ds_write_b32 v4, v121 offset:15048
	ds_write_b32 v4, v122 offset:15312
	ds_write_b32 v4, v123 offset:15576
	ds_write_b32 v4, v124 offset:15840
	ds_write_b32 v4, v125 offset:16104
	ds_write_b32 v4, v126 offset:16368
	ds_write_b32 v4, v127 offset:16632
	s_addk_i32 s42, 0x400
	s_cmp_lt_u32 s42, s43
	s_cbranch_scc0 .Lcv_nonext
	s_cmp_lt_u32 s42, s44
	s_cbranch_scc0 .Lcv_dn1
	s_lshr_b32 s4, s42, 9
	s_add_i32 s4, s4, s45
	s_bfe_u32 s5, s42, 0x30006
	s_and_b32 vcc_lo, s42, 63
	s_lshl_b32 s46, s4, 23
	s_lshl_b32 s47, s5, 20
	s_add_u32 s46, s46, s47
	s_lshl_b32 s47, vcc_lo, 7
	s_add_u32 s46, s46, s47
	s_add_u32 s46, s46, s6
	s_addc_u32 s47, s7, 0
	s_lshl_b32 s52, s4, 21
	s_add_u32 s52, s52, 0x4400000
	s_lshl_b32 s53, s5, 7
	s_add_u32 s52, s52, s53
	s_bfe_u32 s53, vcc_lo, 0x30002
	s_lshl_b32 s53, s53, 18
	s_add_u32 s52, s52, s53
	s_lshr_b32 s53, vcc_lo, 5
	s_lshl_b32 s53, s53, 17
	s_add_u32 s52, s52, s53
	s_and_b32 s53, vcc_lo, 3
	s_lshl_b32 s53, s53, 15
	s_add_u32 s52, s52, s53
	s_add_u32 s52, s52, s10
	s_addc_u32 s53, s11, 0
	s_mov_b32 s51, 0x42000000
	s_movk_i32 s5, 0x2000
	s_movk_i32 s4, 0x4000
	s_branch .Lcv_ld1

.Lcv_ld1:
	v_mad_u32_u24 v12, v15, s5, v14
	global_load_dword v64, v12, s[46:47]
	s_add_u32 s46, s46, s4
	s_addc_u32 s47, s47, 0
	global_load_dword v65, v12, s[46:47]
	s_add_u32 s46, s46, s4
	s_addc_u32 s47, s47, 0
	global_load_dword v66, v12, s[46:47]
	s_add_u32 s46, s46, s4
	s_addc_u32 s47, s47, 0
	global_load_dword v67, v12, s[46:47]
	s_add_u32 s46, s46, s4
	s_addc_u32 s47, s47, 0
	global_load_dword v68, v12, s[46:47]
	s_add_u32 s46, s46, s4
	s_addc_u32 s47, s47, 0
	global_load_dword v69, v12, s[46:47]
	s_add_u32 s46, s46, s4
	s_addc_u32 s47, s47, 0
	global_load_dword v70, v12, s[46:47]
	s_add_u32 s46, s46, s4
	s_addc_u32 s47, s47, 0
	global_load_dword v71, v12, s[46:47]
	s_add_u32 s46, s46, s4
	s_addc_u32 s47, s47, 0
	global_load_dword v72, v12, s[46:47]
	s_add_u32 s46, s46, s4
	s_addc_u32 s47, s47, 0
	global_load_dword v73, v12, s[46:47]
	s_add_u32 s46, s46, s4
	s_addc_u32 s47, s47, 0
	global_load_dword v74, v12, s[46:47]
	s_add_u32 s46, s46, s4
	s_addc_u32 s47, s47, 0
	global_load_dword v75, v12, s[46:47]
	s_add_u32 s46, s46, s4
	s_addc_u32 s47, s47, 0
	global_load_dword v76, v12, s[46:47]
	s_add_u32 s46, s46, s4
	s_addc_u32 s47, s47, 0
	global_load_dword v77, v12, s[46:47]
	s_add_u32 s46, s46, s4
	s_addc_u32 s47, s47, 0
	global_load_dword v78, v12, s[46:47]
	s_add_u32 s46, s46, s4
	s_addc_u32 s47, s47, 0
	global_load_dword v79, v12, s[46:47]
	s_add_u32 s46, s46, s4
	s_addc_u32 s47, s47, 0
	global_load_dword v80, v12, s[46:47]
	s_add_u32 s46, s46, s4
	s_addc_u32 s47, s47, 0
	global_load_dword v81, v12, s[46:47]
	s_add_u32 s46, s46, s4
	s_addc_u32 s47, s47, 0
	global_load_dword v82, v12, s[46:47]
	s_add_u32 s46, s46, s4
	s_addc_u32 s47, s47, 0
	global_load_dword v83, v12, s[46:47]
	s_add_u32 s46, s46, s4
	s_addc_u32 s47, s47, 0
	global_load_dword v84, v12, s[46:47]
	s_add_u32 s46, s46, s4
	s_addc_u32 s47, s47, 0
	global_load_dword v85, v12, s[46:47]
	s_add_u32 s46, s46, s4
	s_addc_u32 s47, s47, 0
	global_load_dword v86, v12, s[46:47]
	s_add_u32 s46, s46, s4
	s_addc_u32 s47, s47, 0
	global_load_dword v87, v12, s[46:47]
	s_add_u32 s46, s46, s4
	s_addc_u32 s47, s47, 0
	global_load_dword v88, v12, s[46:47]
	s_add_u32 s46, s46, s4
	s_addc_u32 s47, s47, 0
	global_load_dword v89, v12, s[46:47]
	s_add_u32 s46, s46, s4
	s_addc_u32 s47, s47, 0
	global_load_dword v90, v12, s[46:47]
	s_add_u32 s46, s46, s4
	s_addc_u32 s47, s47, 0
	global_load_dword v91, v12, s[46:47]
	s_add_u32 s46, s46, s4
	s_addc_u32 s47, s47, 0
	global_load_dword v92, v12, s[46:47]
	s_add_u32 s46, s46, s4
	s_addc_u32 s47, s47, 0
	global_load_dword v93, v12, s[46:47]
	s_add_u32 s46, s46, s4
	s_addc_u32 s47, s47, 0
	global_load_dword v94, v12, s[46:47]
	s_add_u32 s46, s46, s4
	s_addc_u32 s47, s47, 0
	global_load_dword v95, v12, s[46:47]
	s_add_u32 s46, s46, s4
	s_addc_u32 s47, s47, 0
	global_load_dword v96, v12, s[46:47]
	s_add_u32 s46, s46, s4
	s_addc_u32 s47, s47, 0
	global_load_dword v97, v12, s[46:47]
	s_add_u32 s46, s46, s4
	s_addc_u32 s47, s47, 0
	global_load_dword v98, v12, s[46:47]
	s_add_u32 s46, s46, s4
	s_addc_u32 s47, s47, 0
	global_load_dword v99, v12, s[46:47]
	s_add_u32 s46, s46, s4
	s_addc_u32 s47, s47, 0
	global_load_dword v100, v12, s[46:47]
	s_add_u32 s46, s46, s4
	s_addc_u32 s47, s47, 0
	global_load_dword v101, v12, s[46:47]
	s_add_u32 s46, s46, s4
	s_addc_u32 s47, s47, 0
	global_load_dword v102, v12, s[46:47]
	s_add_u32 s46, s46, s4
	s_addc_u32 s47, s47, 0
	global_load_dword v103, v12, s[46:47]
	s_add_u32 s46, s46, s4
	s_addc_u32 s47, s47, 0
	global_load_dword v104, v12, s[46:47]
	s_add_u32 s46, s46, s4
	s_addc_u32 s47, s47, 0
	global_load_dword v105, v12, s[46:47]
	s_add_u32 s46, s46, s4
	s_addc_u32 s47, s47, 0
	global_load_dword v106, v12, s[46:47]
	s_add_u32 s46, s46, s4
	s_addc_u32 s47, s47, 0
	global_load_dword v107, v12, s[46:47]
	s_add_u32 s46, s46, s4
	s_addc_u32 s47, s47, 0
	global_load_dword v108, v12, s[46:47]
	s_add_u32 s46, s46, s4
	s_addc_u32 s47, s47, 0
	global_load_dword v109, v12, s[46:47]
	s_add_u32 s46, s46, s4
	s_addc_u32 s47, s47, 0
	global_load_dword v110, v12, s[46:47]
	s_add_u32 s46, s46, s4
	s_addc_u32 s47, s47, 0
	global_load_dword v111, v12, s[46:47]
	s_add_u32 s46, s46, s4
	s_addc_u32 s47, s47, 0
	global_load_dword v112, v12, s[46:47]
	s_add_u32 s46, s46, s4
	s_addc_u32 s47, s47, 0
	global_load_dword v113, v12, s[46:47]
	s_add_u32 s46, s46, s4
	s_addc_u32 s47, s47, 0
	global_load_dword v114, v12, s[46:47]
	s_add_u32 s46, s46, s4
	s_addc_u32 s47, s47, 0
	global_load_dword v115, v12, s[46:47]
	s_add_u32 s46, s46, s4
	s_addc_u32 s47, s47, 0
	global_load_dword v116, v12, s[46:47]
	s_add_u32 s46, s46, s4
	s_addc_u32 s47, s47, 0
	global_load_dword v117, v12, s[46:47]
	s_add_u32 s46, s46, s4
	s_addc_u32 s47, s47, 0
	global_load_dword v118, v12, s[46:47]
	s_add_u32 s46, s46, s4
	s_addc_u32 s47, s47, 0
	global_load_dword v119, v12, s[46:47]
	s_add_u32 s46, s46, s4
	s_addc_u32 s47, s47, 0
	global_load_dword v120, v12, s[46:47]
	s_add_u32 s46, s46, s4
	s_addc_u32 s47, s47, 0
	global_load_dword v121, v12, s[46:47]
	s_add_u32 s46, s46, s4
	s_addc_u32 s47, s47, 0
	global_load_dword v122, v12, s[46:47]
	s_add_u32 s46, s46, s4
	s_addc_u32 s47, s47, 0
	global_load_dword v123, v12, s[46:47]
	s_add_u32 s46, s46, s4
	s_addc_u32 s47, s47, 0
	global_load_dword v124, v12, s[46:47]
	s_add_u32 s46, s46, s4
	s_addc_u32 s47, s47, 0
	global_load_dword v125, v12, s[46:47]
	s_add_u32 s46, s46, s4
	s_addc_u32 s47, s47, 0
	global_load_dword v126, v12, s[46:47]
	s_add_u32 s46, s46, s4
	s_addc_u32 s47, s47, 0
	global_load_dword v127, v12, s[46:47]
.Lcv_nonext:
	s_waitcnt lgkmcnt(0)
	ds_read_b32 v16, v5
	ds_read_b32 v17, v5 offset:132
	ds_read_b32 v18, v5 offset:264
	ds_read_b32 v19, v5 offset:396
	ds_read_b32 v20, v5 offset:528
	ds_read_b32 v21, v5 offset:660
	ds_read_b32 v22, v5 offset:792
	ds_read_b32 v23, v5 offset:924
	ds_read_b32 v24, v5 offset:1056
	ds_read_b32 v25, v5 offset:1188
	ds_read_b32 v26, v5 offset:1320
	ds_read_b32 v27, v5 offset:1452
	ds_read_b32 v28, v5 offset:1584
	ds_read_b32 v29, v5 offset:1716
	ds_read_b32 v30, v5 offset:1848
	ds_read_b32 v31, v5 offset:1980
	ds_read_b32 v32, v5 offset:32
	ds_read_b32 v33, v5 offset:164
	ds_read_b32 v34, v5 offset:296
	ds_read_b32 v35, v5 offset:428
	ds_read_b32 v36, v5 offset:560
	ds_read_b32 v37, v5 offset:692
	ds_read_b32 v38, v5 offset:824
	ds_read_b32 v39, v5 offset:956
	ds_read_b32 v40, v5 offset:1088
	ds_read_b32 v41, v5 offset:1220
	ds_read_b32 v42, v5 offset:1352
	ds_read_b32 v43, v5 offset:1484
	ds_read_b32 v44, v5 offset:1616
	ds_read_b32 v45, v5 offset:1748
	ds_read_b32 v46, v5 offset:1880
	ds_read_b32 v47, v5 offset:2012
	s_waitcnt lgkmcnt(0)
	v_mul_f32_e32 v16, s50, v16
	v_mul_f32_e32 v17, s50, v17
	v_mul_f32_e32 v18, s50, v18
	v_mul_f32_e32 v19, s50, v19
	v_mul_f32_e32 v20, s50, v20
	v_mul_f32_e32 v21, s50, v21
	v_mul_f32_e32 v22, s50, v22
	v_mul_f32_e32 v23, s50, v23
	v_mul_f32_e32 v24, s50, v24
	v_mul_f32_e32 v25, s50, v25
	v_mul_f32_e32 v26, s50, v26
	v_mul_f32_e32 v27, s50, v27
	v_mul_f32_e32 v28, s50, v28
	v_mul_f32_e32 v29, s50, v29
	v_mul_f32_e32 v30, s50, v30
	v_mul_f32_e32 v31, s50, v31
	v_mul_f32_e32 v32, s50, v32
	v_mul_f32_e32 v33, s50, v33
	v_mul_f32_e32 v34, s50, v34
	v_mul_f32_e32 v35, s50, v35
	v_mul_f32_e32 v36, s50, v36
	v_mul_f32_e32 v37, s50, v37
	v_mul_f32_e32 v38, s50, v38
	v_mul_f32_e32 v39, s50, v39
	v_mul_f32_e32 v40, s50, v40
	v_mul_f32_e32 v41, s50, v41
	v_mul_f32_e32 v42, s50, v42
	v_mul_f32_e32 v43, s50, v43
	v_mul_f32_e32 v44, s50, v44
	v_mul_f32_e32 v45, s50, v45
	v_mul_f32_e32 v46, s50, v46
	v_mul_f32_e32 v47, s50, v47
	v_cvt_pk_fp8_f32 v48, v16, v17
	v_cvt_pk_fp8_f32 v49, v20, v21
	v_cvt_pk_fp8_f32 v50, v24, v25
	v_cvt_pk_fp8_f32 v51, v28, v29
	v_cvt_pk_fp8_f32 v52, v32, v33
	v_cvt_pk_fp8_f32 v53, v36, v37
	v_cvt_pk_fp8_f32 v54, v40, v41
	v_cvt_pk_fp8_f32 v55, v44, v45
	v_cvt_pk_fp8_f32 v48, v18, v19 op_sel:[0,0,1]
	v_cvt_pk_fp8_f32 v49, v22, v23 op_sel:[0,0,1]
	v_cvt_pk_fp8_f32 v50, v26, v27 op_sel:[0,0,1]
	v_cvt_pk_fp8_f32 v51, v30, v31 op_sel:[0,0,1]
	v_cvt_pk_fp8_f32 v52, v34, v35 op_sel:[0,0,1]
	v_cvt_pk_fp8_f32 v53, v38, v39 op_sel:[0,0,1]
	v_cvt_pk_fp8_f32 v54, v42, v43 op_sel:[0,0,1]
	v_cvt_pk_fp8_f32 v55, v46, v47 op_sel:[0,0,1]
	ds_read_b32 v16, v5 offset:64
	ds_read_b32 v17, v5 offset:196
	ds_read_b32 v18, v5 offset:328
	ds_read_b32 v19, v5 offset:460
	ds_read_b32 v20, v5 offset:592
	ds_read_b32 v21, v5 offset:724
	ds_read_b32 v22, v5 offset:856
	ds_read_b32 v23, v5 offset:988
	ds_read_b32 v24, v5 offset:1120
	ds_read_b32 v25, v5 offset:1252
	ds_read_b32 v26, v5 offset:1384
	ds_read_b32 v27, v5 offset:1516
	ds_read_b32 v28, v5 offset:1648
	ds_read_b32 v29, v5 offset:1780
	ds_read_b32 v30, v5 offset:1912
	ds_read_b32 v31, v5 offset:2044
	ds_read_b32 v32, v5 offset:96
	ds_read_b32 v33, v5 offset:228
	ds_read_b32 v34, v5 offset:360
	ds_read_b32 v35, v5 offset:492
	ds_read_b32 v36, v5 offset:624
	ds_read_b32 v37, v5 offset:756
	ds_read_b32 v38, v5 offset:888
	ds_read_b32 v39, v5 offset:1020
	ds_read_b32 v40, v5 offset:1152
	ds_read_b32 v41, v5 offset:1284
	ds_read_b32 v42, v5 offset:1416
	ds_read_b32 v43, v5 offset:1548
	ds_read_b32 v44, v5 offset:1680
	ds_read_b32 v45, v5 offset:1812
	ds_read_b32 v46, v5 offset:1944
	ds_read_b32 v47, v5 offset:2076
	s_waitcnt lgkmcnt(0)
	v_mul_f32_e32 v16, s50, v16
	v_mul_f32_e32 v17, s50, v17
	v_mul_f32_e32 v18, s50, v18
	v_mul_f32_e32 v19, s50, v19
	v_mul_f32_e32 v20, s50, v20
	v_mul_f32_e32 v21, s50, v21
	v_mul_f32_e32 v22, s50, v22
	v_mul_f32_e32 v23, s50, v23
	v_mul_f32_e32 v24, s50, v24
	v_mul_f32_e32 v25, s50, v25
	v_mul_f32_e32 v26, s50, v26
	v_mul_f32_e32 v27, s50, v27
	v_mul_f32_e32 v28, s50, v28
	v_mul_f32_e32 v29, s50, v29
	v_mul_f32_e32 v30, s50, v30
	v_mul_f32_e32 v31, s50, v31
	v_mul_f32_e32 v32, s50, v32
	v_mul_f32_e32 v33, s50, v33
	v_mul_f32_e32 v34, s50, v34
	v_mul_f32_e32 v35, s50, v35
	v_mul_f32_e32 v36, s50, v36
	v_mul_f32_e32 v37, s50, v37
	v_mul_f32_e32 v38, s50, v38
	v_mul_f32_e32 v39, s50, v39
	v_mul_f32_e32 v40, s50, v40
	v_mul_f32_e32 v41, s50, v41
	v_mul_f32_e32 v42, s50, v42
	v_mul_f32_e32 v43, s50, v43
	v_mul_f32_e32 v44, s50, v44
	v_mul_f32_e32 v45, s50, v45
	v_mul_f32_e32 v46, s50, v46
	v_mul_f32_e32 v47, s50, v47
	v_cvt_pk_fp8_f32 v56, v16, v17
	v_cvt_pk_fp8_f32 v57, v20, v21
	v_cvt_pk_fp8_f32 v58, v24, v25
	v_cvt_pk_fp8_f32 v59, v28, v29
	v_cvt_pk_fp8_f32 v60, v32, v33
	v_cvt_pk_fp8_f32 v61, v36, v37
	v_cvt_pk_fp8_f32 v62, v40, v41
	v_cvt_pk_fp8_f32 v63, v44, v45
	v_cvt_pk_fp8_f32 v56, v18, v19 op_sel:[0,0,1]
	v_cvt_pk_fp8_f32 v57, v22, v23 op_sel:[0,0,1]
	v_cvt_pk_fp8_f32 v58, v26, v27 op_sel:[0,0,1]
	v_cvt_pk_fp8_f32 v59, v30, v31 op_sel:[0,0,1]
	v_cvt_pk_fp8_f32 v60, v34, v35 op_sel:[0,0,1]
	v_cvt_pk_fp8_f32 v61, v38, v39 op_sel:[0,0,1]
	v_cvt_pk_fp8_f32 v62, v42, v43 op_sel:[0,0,1]
	v_cvt_pk_fp8_f32 v63, v46, v47 op_sel:[0,0,1]
	s_nop 0
	global_store_dwordx4 v6, v[48:51], s[48:49]
	global_store_dwordx4 v7, v[52:55], s[48:49]
	global_store_dwordx4 v8, v[56:59], s[48:49]
	global_store_dwordx4 v9, v[60:63], s[48:49]
	s_cmp_lt_u32 s42, s43
	s_cbranch_scc1 .Lcv_loop
.Lcv_done:
	s_waitcnt vmcnt(0) lgkmcnt(0)

c_jobs:
	.long	4
	.long	2840
	.long	1024
	.long	0
	.long	1024
	.long	0
	.long	1
	.long	2
	.quad	2908160
	.quad	2097152
	.quad	2097152
	.long	0
	.long	0
	.long	4
	.long	2840
	.long	1024
	.long	1536
	.long	512
	.long	1024
	.long	1
	.long	2
	.quad	2908160
	.quad	2097152
	.quad	2097152
	.long	0
	.long	0
	.long	4
	.long	2840
	.long	1024
	.long	2048
	.long	128
	.long	1536
	.long	1
	.long	2
	.quad	2908160
	.quad	2097152
	.quad	2097152
	.long	0
	.long	0
	.long	4
	.long	2840
	.long	1024
	.long	2176
	.long	128
	.long	1664
	.long	1
	.long	2
	.quad	2908160
	.quad	2097152
	.quad	2097152
	.long	0
	.long	0
	.long	4
	.long	2840
	.long	1024
	.long	2304
	.long	128
	.long	1792
	.long	1
	.long	2
	.quad	2908160
	.quad	2097152
	.quad	2097152
	.long	0
	.long	0
	.long	4
	.long	2840
	.long	1024
	.long	2560
	.long	128
	.long	1920
	.long	1
	.long	2
	.quad	2908160
	.quad	2097152
	.quad	2097152
	.long	0
	.long	0
	.long	4
	.long	2840
	.long	1024
	.long	1024
	.long	512
	.long	0
	.long	0
	.long	2
	.quad	2908160
	.quad	10485760
	.quad	786432
	.long	0
	.long	0
	.long	4
	.long	2840
	.long	1024
	.long	2432
	.long	128
	.long	512
	.long	0
	.long	2
	.quad	2908160
	.quad	10485760
	.quad	786432
	.long	0
	.long	0
	.long	4
	.long	2840
	.long	1024
	.long	2688
	.long	128
	.long	640
	.long	0
	.long	2
	.quad	2908160
	.quad	10485760
	.quad	786432
	.long	0
	.long	0
	.long	5
	.long	1024
	.long	1024
	.long	0
	.long	1024
	.long	0
	.long	0
	.long	2
	.quad	1048576
	.quad	13631488
	.quad	1048576
	.long	64
	.long	0
	.long	13
	.long	256
	.long	2048
	.long	0
	.long	256
	.long	0
	.long	0
	.long	4
	.quad	524288
	.quad	17825792
	.quad	524288
	.long	0
	.long	0
	.long	15
	.long	6144
	.long	1024
	.long	0
	.long	2048
	.long	0
	.long	0
	.long	2
	.quad	6291456
	.quad	22020096
	.quad	4194304
	.long	32
	.long	0
	.long	15
	.long	6144
	.long	1024
	.long	4096
	.long	2048
	.long	2048
	.long	0
	.long	2
	.quad	6291456
	.quad	22020096
	.quad	4194304
	.long	32
	.long	0
	.long	15
	.long	6144
	.long	1024
	.long	2048
	.long	2048
	.long	0
	.long	0
	.long	2
	.quad	6291456
	.quad	38797312
	.quad	2097152
	.long	32
	.long	0
	.long	16
	.long	1024
	.long	2048
	.long	0
	.long	1024
	.long	0
	.long	0
	.long	2
	.quad	2097152
	.quad	51380224
	.quad	2097152
	.long	128
	.long	0
	.long	20
	.long	2048
	.long	1024
	.long	0
	.long	2048
	.long	0
	.long	2
	.long	64
	.quad	2097152
	.quad	71303168
	.quad	2097152
	.long	32
	.long	0
	.long	22
	.long	1024
	.long	1024
	.long	0
	.long	1024
	.long	0
	.long	0
	.long	64
	.quad	1048576
	.quad	608174080
	.quad	1048576
	.long	64
	.long	0
	.long	24
	.long	1024
	.long	256
	.long	0
	.long	1024
	.long	0
	.long	0
	.long	4
	.quad	262144
	.quad	59768832
	.quad	262144
	.long	0
	.long	0
	.long	25
	.long	1024
	.long	1024
	.long	0
	.long	1024
	.long	0
	.long	0
	.long	4
	.quad	1048576
	.quad	61865984
	.quad	1048576
	.long	32
	.long	0
	.size	c_jobs, 1216

	.type	__hip_cuid_b50e1a6430de2f85,@object
